# baseline (speedup 1.0000x reference)
_Z11attn_kernelPKDF16_S0_PDF16_:
	s_load_dwordx4 s[4:7], s[0:1], 0x0
	s_load_dwordx2 s[8:9], s[0:1], 0x10
	s_lshr_b32 s1, s2, 3
	s_lshr_b32 s10, s2, 7
	s_and_b32 s0, s2, 4
	s_and_b32 s1, s1, 8
	s_and_b32 s20, s2, 3
	s_lshl_b32 s30, s10, 4
	s_or_b32 s22, s1, s0
	s_or_b32 s0, s30, s20
	s_or_b32 s14, s0, s22
	s_or_b32 s0, s20, 16
	s_sub_i32 s0, s0, s30
	s_mov_b32 s15, 0
	s_or_b32 s0, s0, s22
	s_bfe_u32 s24, s2, 0x30003
	s_ashr_i32 s1, s0, 31
	s_lshl_b64 s[2:3], s[14:15], 18
	s_waitcnt lgkmcnt(0)
	s_add_u32 s2, s4, s2
	s_addc_u32 s3, s5, s3
	s_lshl_b64 s[0:1], s[0:1], 18
	s_add_u32 s11, s4, s0
	s_addc_u32 s12, s5, s1
	s_add_u32 s13, s6, s0
	v_readfirstlane_b32 s16, v0
	s_addc_u32 s18, s7, s1
	s_lshl_b32 s0, s24, 2
	s_lshr_b32 s1, s16, 7
	s_add_i32 s14, s1, s0
	s_lshr_b32 s23, s16, 6
	s_lshl_b64 s[0:1], s[14:15], 13
	s_add_u32 s0, s2, s0
	v_and_b32_e32 v189, 31, v0
	s_addc_u32 s1, s3, s1
	s_lshl_b32 s21, s23, 5
	v_and_or_b32 v1, s21, 32, v189
	v_lshlrev_b32_e32 v186, 4, v1
	v_mov_b32_e32 v187, 0
	s_lshl_b32 s14, s23, 9
	v_lshl_add_u64 v[2:3], s[0:1], 0, v[186:187]
	s_and_b32 s0, s16, 0x3fffffc0
	s_lshl_b64 s[16:17], s[14:15], 1
	v_and_b32_e32 v188, 63, v0
	s_add_u32 s2, s11, s16
	s_addc_u32 s3, s12, s17
	s_add_u32 s44, s2, 0x8000
	s_addc_u32 s45, s3, 0
	v_lshlrev_b32_e32 v186, 4, v188
	v_lshl_add_u64 v[44:45], s[2:3], 0, v[186:187]
	s_add_u32 s2, s13, s16
	s_addc_u32 s3, s18, s17
	s_add_u32 s46, s2, 0x6000
	s_addc_u32 s47, s3, 0
	s_lshl_b32 s25, s23, 10
	s_cmp_lg_u32 0, -1
	s_cselect_b32 s1, 0, 0
	v_bfe_u32 v46, v0, 5, 1
	s_add_i32 s25, s25, s1
	s_mov_b32 s1, m0
	s_mov_b32 m0, s25
	s_nop 0
	global_load_lds_dwordx4 v[44:45], off
	s_mov_b32 m0, s1
	v_lshl_add_u64 v[34:35], s[2:3], 0, v[186:187]
	s_add_i32 s26, s25, 0x6000
	v_lshlrev_b32_e32 v4, 10, v46
	s_mov_b32 s1, m0
	s_mov_b32 m0, s26
	s_nop 0
	global_load_lds_dwordx4 v[34:35], off
	s_mov_b32 m0, s1
	s_mov_b64 s[18:19], 0x2000
	v_mov_b32_e32 v5, v187
	v_lshl_add_u64 v[6:7], v[44:45], 0, s[18:19]
	s_add_i32 s1, s25, 0x2000
	s_mov_b32 s2, m0
	s_mov_b32 m0, s1
	s_nop 0
	global_load_lds_dwordx4 v[6:7], off
	s_mov_b32 m0, s2
	v_lshl_add_u64 v[2:3], v[2:3], 0, v[4:5]
	global_load_dwordx4 v[136:139], v[2:3], off
	global_load_dwordx4 v[128:131], v[2:3], off offset:2048
	s_movk_i32 s1, 0x1000
	v_add_co_u32_e32 v2, vcc, s1, v2
	v_lshlrev_b32_e32 v1, 4, v189
	s_nop 0
	v_addc_co_u32_e32 v3, vcc, 0, v3, vcc
	global_load_dwordx4 v[120:123], v[2:3], off
	global_load_dwordx4 v[112:115], v[2:3], off offset:2048
	v_add3_u32 v184, 0, v4, v1
	v_mov_b32_e32 v2, v187
	v_mov_b32_e32 v3, v187
	v_mov_b32_e32 v4, v187
	v_mov_b32_e32 v6, v187
	v_mov_b32_e32 v7, v187
	v_mov_b32_e32 v8, v187
	v_mov_b32_e32 v9, v187
	v_mov_b32_e32 v10, v187
	v_mov_b32_e32 v11, v187
	v_mov_b32_e32 v12, v187
	v_mov_b32_e32 v13, v187
	v_mov_b32_e32 v14, v187
	v_mov_b32_e32 v15, v187
	v_mov_b32_e32 v16, v187
	v_mov_b32_e32 v17, v187
	s_mov_b64 s[2:3], 0x4000
	v_lshl_add_u64 v[18:19], v[44:45], 0, s[2:3]
	s_add_i32 s1, s25, 0x4000
	s_mov_b32 s11, m0
	s_mov_b32 m0, s1
	s_nop 0
	global_load_lds_dwordx4 v[18:19], off
	s_mov_b32 m0, s11
	v_lshl_add_u64 v[18:19], v[34:35], 0, s[18:19]
	s_add_i32 s1, s25, 0x8000
	s_mov_b32 s11, m0
	s_mov_b32 m0, s1
	s_nop 0
	global_load_lds_dwordx4 v[18:19], off
	s_mov_b32 m0, s11
	s_waitcnt vmcnt(4) lgkmcnt(0)
	s_barrier
	ds_read_b128 v[36:39], v184
	ds_read_b128 v[40:43], v184 offset:512
	v_lshlrev_b32_e32 v190, 3, v0
	s_mov_b64 s[12:13], 0x6000
	s_or_b32 s14, s22, s20
	s_sub_i32 s14, s14, s30
	s_add_i32 s34, s14, 16
	s_lshl_b32 s0, s0, 2
	s_ashr_i32 s35, s34, 31
	s_lshl_b64 s[34:35], s[34:35], 18
	s_mov_b32 s27, -1
	s_waitcnt vmcnt(3) lgkmcnt(1)
	v_mfma_f32_32x32x16_f16 v[18:33], v[36:39], v[136:139], v[2:17]
	s_movk_i32 s28, 0x6000
	s_movk_i32 s31, 0x2000
	s_movk_i32 s29, 0x4000
	v_lshlrev_b32_e32 v191, 9, v46
	v_lshlrev_b32_e32 v182, 4, v46
	v_lshlrev_b32_e32 v180, 4, v188
	s_waitcnt lgkmcnt(0)
	v_mfma_f32_32x32x16_f16 v[2:17], v[40:43], v[136:139], v[2:17]
	ds_read_b128 v[36:39], v184 offset:2048
	ds_read_b128 v[40:43], v184 offset:2560
	s_waitcnt vmcnt(2) lgkmcnt(1)
	v_mfma_f32_32x32x16_f16 v[18:33], v[36:39], v[128:131], v[18:33]
	s_waitcnt lgkmcnt(0)
	v_mfma_f32_32x32x16_f16 v[2:17], v[40:43], v[128:131], v[2:17]
	ds_read_b128 v[36:39], v184 offset:4096
	ds_read_b128 v[40:43], v184 offset:4608
	s_waitcnt vmcnt(1) lgkmcnt(1)
	v_mfma_f32_32x32x16_f16 v[18:33], v[36:39], v[120:123], v[18:33]
	s_waitcnt lgkmcnt(0)
	v_mfma_f32_32x32x16_f16 v[2:17], v[40:43], v[120:123], v[2:17]
	ds_read_b128 v[36:39], v184 offset:6144
	ds_read_b128 v[40:43], v184 offset:6656
	s_waitcnt vmcnt(0) lgkmcnt(1)
	v_mfma_f32_32x32x16_f16 v[18:33], v[36:39], v[112:115], v[18:33]
	s_waitcnt lgkmcnt(0)
	v_mfma_f32_32x32x16_f16 v[2:17], v[40:43], v[112:115], v[2:17]
	s_nop 11
	v_max_f32_e32 v1, v19, v18
	v_max3_f32 v37, v20, v21, v3
	v_max3_f32 v1, v1, v2, v4
	v_max3_f32 v36, v37, v24, v25
	v_max3_f32 v1, v1, v5, v22
	v_max3_f32 v36, v36, v8, v9
	v_max3_f32 v1, v1, v23, v6
	v_max3_f32 v36, v36, v28, v29
	v_max3_f32 v1, v1, v7, v26
	v_max3_f32 v36, v36, v12, v13
	v_max3_f32 v1, v1, v27, v10
	v_max3_f32 v36, v36, v32, v33
	v_max3_f32 v1, v1, v11, v30
	v_max3_f32 v36, v36, v16, v17
	v_max3_f32 v1, v1, v31, v14
	v_max3_f32 v1, v1, v15, v36
	v_mov_b32_e32 v36, v1
	s_nop 1
	v_permlane32_swap_b32_e32 v1, v36
	v_max_f32_e32 v183, v36, v1
	v_lshlrev_b32_e32 v1, 1, v0
	v_sub_f32_e32 v36, v2, v183
	v_and_b32_e32 v1, 32, v1
	v_and_b32_e32 v2, 24, v190
	v_lshlrev_b32_e32 v0, 4, v0
	v_add3_u32 v1, 0, v1, v2
	v_and_b32_e32 v0, 0xc0, v0
	v_lshlrev_b32_e32 v2, 8, v46
	v_add3_u32 v181, v1, v2, v0
	v_xor_b32_e32 v0, 0x80000000, v183
	v_sub_f32_e32 v37, v3, v183
	v_sub_f32_e32 v38, v4, v183
	v_sub_f32_e32 v39, v5, v183
	v_sub_f32_e32 v40, v6, v183
	v_sub_f32_e32 v41, v7, v183
	v_sub_f32_e32 v42, v8, v183
	v_sub_f32_e32 v43, v9, v183
	v_sub_f32_e32 v47, v10, v183
	v_sub_f32_e32 v57, v11, v183
	v_sub_f32_e32 v58, v12, v183
	v_sub_f32_e32 v59, v13, v183
	v_sub_f32_e32 v60, v14, v183
	v_sub_f32_e32 v61, v15, v183
	v_mov_b32_e32 v1, v0
	v_mov_b32_e32 v2, v0
	v_mov_b32_e32 v3, v0
	v_mov_b32_e32 v4, v0
	v_mov_b32_e32 v5, v0
	v_mov_b32_e32 v6, v0
	v_mov_b32_e32 v7, v0
	v_mov_b32_e32 v8, v0
	v_mov_b32_e32 v9, v0
	v_mov_b32_e32 v10, v0
	v_mov_b32_e32 v11, v0
	v_mov_b32_e32 v12, v0
	v_mov_b32_e32 v13, v0
	v_mov_b32_e32 v14, v0
	v_mov_b32_e32 v15, v0
	s_waitcnt vmcnt(0) lgkmcnt(0)
	s_barrier
	v_sub_f32_e32 v62, v16, v183
	v_sub_f32_e32 v63, v17, v183
	v_lshl_add_u64 v[16:17], v[44:45], 0, s[12:13]
	s_mov_b32 s1, m0
	s_mov_b32 m0, s25
	s_nop 0
	global_load_lds_dwordx4 v[16:17], off
	s_mov_b32 m0, s1
	s_add_i32 s1, s25, 0xa000
	v_lshl_add_u64 v[16:17], v[34:35], 0, s[2:3]
	s_mov_b32 s11, m0
	s_mov_b32 m0, s1
	s_nop 0
	global_load_lds_dwordx4 v[16:17], off
	s_mov_b32 m0, s11
	ds_read_b128 v[172:175], v184 offset:8192
	ds_read_b128 v[168:171], v184 offset:8704
	ds_read_b128 v[164:167], v184 offset:10240
	ds_read_b128 v[160:163], v184 offset:10752
	ds_read_b128 v[156:159], v184 offset:12288
	ds_read_b128 v[152:155], v184 offset:12800
	ds_read_b128 v[148:151], v184 offset:14336
	ds_read_b128 v[144:147], v184 offset:14848
	s_add_i32 s11, s0, 0
	v_sub_f32_e32 v18, v18, v183
	v_sub_f32_e32 v19, v19, v183
	v_sub_f32_e32 v20, v20, v183
	v_sub_f32_e32 v21, v21, v183
	v_sub_f32_e32 v22, v22, v183
	v_sub_f32_e32 v23, v23, v183
	v_sub_f32_e32 v24, v24, v183
	v_sub_f32_e32 v25, v25, v183
	v_sub_f32_e32 v26, v26, v183
	v_sub_f32_e32 v27, v27, v183
	v_sub_f32_e32 v28, v28, v183
	v_sub_f32_e32 v29, v29, v183
	v_sub_f32_e32 v30, v30, v183
	v_sub_f32_e32 v31, v31, v183
	v_sub_f32_e32 v32, v32, v183
	v_sub_f32_e32 v33, v33, v183
	s_add_u32 s14, s16, s34
	v_exp_f32_e32 v64, v18
	v_exp_f32_e32 v65, v19
	v_exp_f32_e32 v48, v36
	v_exp_f32_e32 v49, v37
	v_exp_f32_e32 v66, v20
	v_exp_f32_e32 v50, v38
	v_exp_f32_e32 v67, v21
	v_exp_f32_e32 v51, v39
	v_exp_f32_e32 v68, v22
	v_exp_f32_e32 v52, v40
	v_exp_f32_e32 v69, v23
	v_exp_f32_e32 v53, v41
	v_exp_f32_e32 v70, v24
	v_exp_f32_e32 v54, v42
	v_exp_f32_e32 v71, v25
	v_exp_f32_e32 v55, v43
	v_exp_f32_e32 v72, v26
	v_exp_f32_e32 v56, v47
	v_exp_f32_e32 v73, v27
	v_exp_f32_e32 v57, v57
	v_exp_f32_e32 v74, v28
	v_exp_f32_e32 v58, v58
	v_exp_f32_e32 v75, v29
	v_exp_f32_e32 v59, v59
	v_exp_f32_e32 v76, v30
	v_exp_f32_e32 v60, v60
	v_exp_f32_e32 v77, v31
	v_exp_f32_e32 v61, v61
	v_exp_f32_e32 v78, v32
	v_exp_f32_e32 v62, v62
	v_exp_f32_e32 v79, v33
	v_exp_f32_e32 v63, v63
	s_addc_u32 s16, s17, s35
	s_waitcnt vmcnt(2) lgkmcnt(0)
	s_barrier
	v_or_b32_e32 v16, s14, v186
	v_mov_b32_e32 v17, s16
	v_lshl_add_u64 v[16:17], v[16:17], 0, s[18:19]
	v_cmp_gt_u32_e64 s[0:1], 32, v188
	s_mov_b32 s16, 0x41000000
	s_mov_b32 s36, 0x43800000
	s_mov_b64 s[4:5], 0x8000
	s_movk_i32 s14, 0x2000
	s_movk_i32 s19, 0x4000
	v_mov_b32_e32 v16, v187
	v_mov_b32_e32 v17, v187
	v_mov_b32_e32 v18, v187
	v_mov_b32_e32 v19, v187
	v_mov_b32_e32 v20, v187
	v_mov_b32_e32 v21, v187
	v_mov_b32_e32 v22, v187
	v_mov_b32_e32 v23, v187
	v_mov_b32_e32 v24, v187
	v_mov_b32_e32 v25, v187
	v_mov_b32_e32 v26, v187
	v_mov_b32_e32 v27, v187
	v_mov_b32_e32 v28, v187
	v_mov_b32_e32 v29, v187
	v_mov_b32_e32 v30, v187
	v_mov_b32_e32 v31, v187
	v_mov_b32_e32 v32, v187
	v_mov_b32_e32 v33, v187
	v_mov_b32_e32 v34, v187
	v_mov_b32_e32 v35, v187
	v_mov_b32_e32 v36, v187
	v_mov_b32_e32 v37, v187
	v_mov_b32_e32 v38, v187
	v_mov_b32_e32 v39, v187
	v_mov_b32_e32 v40, v187
	v_mov_b32_e32 v41, v187
	v_mov_b32_e32 v42, v187
	v_mov_b32_e32 v43, v187
	v_mov_b32_e32 v44, v187
	v_mov_b32_e32 v45, v187
	v_mov_b32_e32 v46, v187
	v_mov_b32_e32 v47, v187
	v_lshl_add_u32 v186, v189, 2, s11
	s_cmp_lt_u32 s23, 4
	s_cbranch_scc1 .Lmy_attn_noprio
	s_setprio 1
.Lmy_attn_noprio:
.LBB2_1:
	v_mfma_f32_32x32x16_f16 v[96:111], v[172:175], v[136:139], v[0:15]
	s_mov_b32 s17, s31
	s_mov_b32 s18, s15
	v_add_u32_e32 v185, s18, v181
	ds_read_b64_tr_b16 v[176:177], v185 offset:24576
	ds_read_b64_tr_b16 v[178:179], v185 offset:25088
	v_add_f32_e32 v80, v64, v65
	v_add_f32_e32 v80, v66, v80
	v_add_f32_e32 v80, v67, v80
	v_add_f32_e32 v80, v68, v80
	v_add_f32_e32 v80, v69, v80
	v_cvt_pk_f16_f32 v140, v64, v65
	v_cvt_pk_f16_f32 v141, v66, v67
	ds_read_b64_tr_b16 v[172:173], v185 offset:28672
	ds_read_b64_tr_b16 v[174:175], v185 offset:29184
	v_add_f32_e32 v64, v70, v80
	s_waitcnt lgkmcnt(10)
	v_mfma_f32_32x32x16_f16 v[80:95], v[168:171], v[136:139], v[0:15]
	v_add_f32_e32 v64, v71, v64
	v_add_f32_e32 v64, v72, v64
	v_add_f32_e32 v64, v73, v64
	v_cvt_pk_f16_f32 v142, v68, v69
	v_cvt_pk_f16_f32 v143, v70, v71
	ds_read_b64_tr_b16 v[68:69], v185 offset:25600
	ds_read_b64_tr_b16 v[70:71], v185 offset:26112
	s_waitcnt lgkmcnt(11)
	v_mfma_f32_32x32x16_f16 v[96:111], v[164:167], v[128:131], v[96:111]
	v_add_f32_e32 v64, v74, v64
	v_add_f32_e32 v64, v75, v64
	v_add_f32_e32 v64, v76, v64
	v_add_f32_e32 v116, v77, v64
	v_cvt_pk_f16_f32 v132, v72, v73
	v_cvt_pk_f16_f32 v133, v74, v75
	ds_read_b64_tr_b16 v[64:65], v185 offset:29696
	ds_read_b64_tr_b16 v[66:67], v185 offset:30208
	s_waitcnt lgkmcnt(12)
	v_mfma_f32_32x32x16_f16 v[80:95], v[160:163], v[128:131], v[80:95]
	v_add_f32_e32 v72, v78, v116
	v_add_f32_e32 v72, v79, v72
	v_add_f32_e32 v72, v48, v72
	v_add_f32_e32 v116, v49, v72
	v_cvt_pk_f16_f32 v134, v76, v77
	v_cvt_pk_f16_f32 v135, v78, v79
	ds_read_b64_tr_b16 v[72:73], v185 offset:26624
	ds_read_b64_tr_b16 v[74:75], v185 offset:27136
	s_waitcnt lgkmcnt(13)
	v_mfma_f32_32x32x16_f16 v[96:111], v[156:159], v[120:123], v[96:111]
	v_add_f32_e32 v76, v50, v116
	v_add_f32_e32 v76, v51, v76
	v_add_f32_e32 v76, v52, v76
	v_add_f32_e32 v76, v53, v76
	v_cvt_pk_f16_f32 v124, v48, v49
	v_cvt_pk_f16_f32 v125, v50, v51
	ds_read_b64_tr_b16 v[48:49], v185 offset:30720
	ds_read_b64_tr_b16 v[50:51], v185 offset:31232
	s_waitcnt lgkmcnt(14)
	v_mfma_f32_32x32x16_f16 v[80:95], v[152:155], v[120:123], v[80:95]
	v_add_f32_e32 v76, v54, v76
	v_add_f32_e32 v76, v55, v76
	v_add_f32_e32 v76, v56, v76
	v_add_f32_e32 v76, v57, v76
	v_cvt_pk_f16_f32 v126, v52, v53
	v_cvt_pk_f16_f32 v127, v54, v55
	ds_read_b64_tr_b16 v[52:53], v185 offset:27648
	ds_read_b64_tr_b16 v[54:55], v185 offset:28160
	s_waitcnt lgkmcnt(14)
	v_mfma_f32_32x32x16_f16 v[96:111], v[148:151], v[112:115], v[96:111]
	v_add_f32_e32 v76, v58, v76
	v_add_f32_e32 v76, v59, v76
	v_add_f32_e32 v76, v60, v76
	v_add_f32_e32 v76, v61, v76
	v_cvt_pk_f16_f32 v116, v56, v57
	v_cvt_pk_f16_f32 v117, v58, v59
	ds_read_b64_tr_b16 v[56:57], v185 offset:31744
	ds_read_b64_tr_b16 v[58:59], v185 offset:32256
	v_mfma_f32_32x32x16_f16 v[80:95], v[144:147], v[112:115], v[80:95]
	v_add_f32_e32 v76, v62, v76
	v_add_f32_e32 v76, v63, v76
	v_cvt_pk_f16_f32 v118, v60, v61
	v_cvt_pk_f16_f32 v119, v62, v63
	s_add_i32 m0, s14, s25
	v_cmp_lt_f32_e32 vcc, s36, v76
	global_load_lds_dwordx4 v180, s[44:45]
	s_add_i32 m0, s28, s26
	s_add_u32 s44, s44, 0x2000
	global_load_lds_dwordx4 v180, s[46:47]
	s_addc_u32 s45, s45, 0
	s_add_u32 s46, s46, 0x2000
	s_addc_u32 s47, s47, 0
	s_cbranch_vccnz .Lmy_rare_1
